# stack: setprio-free GEMM loops + P3 gate loads prefetched in the last K iteration + P4 second-half residual loads issued together
# speedup vs baseline: 1.0006x; 1.0006x over previous
.Lp3_nopf:
	s_barrier
	s_waitcnt lgkmcnt(7)
	v_mfma_f32_16x16x32_bf16 v[130:133], v[140:143], v[172:175], v[130:133]
	v_mfma_f32_16x16x32_bf16 v[126:129], v[148:151], v[172:175], v[126:129]
	s_waitcnt lgkmcnt(5)
	v_mfma_f32_16x16x32_bf16 v[122:125], v[140:143], v[180:183], v[122:125]
	v_mfma_f32_16x16x32_bf16 v[118:121], v[148:151], v[180:183], v[118:121]
	s_waitcnt lgkmcnt(3)
	v_mfma_f32_16x16x32_bf16 v[114:117], v[140:143], v[188:191], v[114:117]
	v_mfma_f32_16x16x32_bf16 v[110:113], v[148:151], v[188:191], v[110:113]
	s_waitcnt lgkmcnt(1)
	v_mfma_f32_16x16x32_bf16 v[106:109], v[140:143], v[196:199], v[106:109]
	v_mfma_f32_16x16x32_bf16 v[102:105], v[148:151], v[196:199], v[102:105]
	v_mfma_f32_16x16x32_bf16 v[130:133], v[144:147], v[176:179], v[130:133]
	v_mfma_f32_16x16x32_bf16 v[126:129], v[152:155], v[176:179], v[126:129]
	v_mfma_f32_16x16x32_bf16 v[122:125], v[144:147], v[184:187], v[122:125]
	v_mfma_f32_16x16x32_bf16 v[118:121], v[152:155], v[184:187], v[118:121]
	v_mfma_f32_16x16x32_bf16 v[114:117], v[144:147], v[192:195], v[114:117]
	v_mfma_f32_16x16x32_bf16 v[110:113], v[152:155], v[192:195], v[110:113]
	s_waitcnt lgkmcnt(0)
	v_mfma_f32_16x16x32_bf16 v[106:109], v[144:147], v[200:203], v[106:109]
	v_mfma_f32_16x16x32_bf16 v[102:105], v[152:155], v[200:203], v[102:105]
	v_mfma_f32_16x16x32_bf16 v[98:101], v[156:159], v[172:175], v[98:101]
	v_mfma_f32_16x16x32_bf16 v[94:97], v[164:167], v[172:175], v[94:97]
	v_mfma_f32_16x16x32_bf16 v[90:93], v[156:159], v[180:183], v[90:93]
	v_mfma_f32_16x16x32_bf16 v[86:89], v[164:167], v[180:183], v[86:89]
	v_mfma_f32_16x16x32_bf16 v[82:85], v[156:159], v[188:191], v[82:85]
	v_mfma_f32_16x16x32_bf16 v[78:81], v[164:167], v[188:191], v[78:81]
	v_mfma_f32_16x16x32_bf16 v[74:77], v[156:159], v[196:199], v[74:77]
	v_mfma_f32_16x16x32_bf16 v[70:73], v[164:167], v[196:199], v[70:73]
	v_mfma_f32_16x16x32_bf16 v[98:101], v[160:163], v[176:179], v[98:101]
	v_mfma_f32_16x16x32_bf16 v[94:97], v[168:171], v[176:179], v[94:97]
	v_mfma_f32_16x16x32_bf16 v[90:93], v[160:163], v[184:187], v[90:93]
	v_mfma_f32_16x16x32_bf16 v[86:89], v[168:171], v[184:187], v[86:89]
	v_mfma_f32_16x16x32_bf16 v[82:85], v[160:163], v[192:195], v[82:85]
	v_mfma_f32_16x16x32_bf16 v[78:81], v[168:171], v[192:195], v[78:81]
	v_mfma_f32_16x16x32_bf16 v[74:77], v[160:163], v[200:203], v[74:77]
	v_mfma_f32_16x16x32_bf16 v[70:73], v[168:171], v[200:203], v[70:73]
	s_barrier
	s_mov_b32 m0, s28
	s_mov_b32 s10, s6
	s_mov_b32 s11, s7
	ds_read_b128 v[172:175], v210 offset:16384
	ds_read_b128 v[176:179], v210 offset:17408
	ds_read_b128 v[180:183], v210 offset:18432
	ds_read_b128 v[184:187], v210 offset:19456
	ds_read_b128 v[188:191], v210 offset:20480
	ds_read_b128 v[192:195], v210 offset:21504
	ds_read_b128 v[196:199], v210 offset:22528
	ds_read_b128 v[200:203], v210 offset:23552
	buffer_load_dwordx4 v135, s[8:11], s61 offen lds
	s_mov_b32 m0, s29
	s_add_i32 s63, s61, 0x80000
	buffer_load_dwordx4 v207, s[8:11], s61 offen lds
	s_mov_b32 m0, s30
	s_nop 0
	buffer_load_dwordx4 v135, s[8:11], s63 offen lds
	s_mov_b32 m0, s31
	s_nop 0
	buffer_load_dwordx4 v207, s[8:11], s63 offen lds
	s_mov_b32 m0, s27
	s_nop 0
	buffer_load_dwordx4 v1, s[4:7], s62 offen lds
	s_mov_b32 m0, s33
	s_nop 0
	buffer_load_dwordx4 v206, s[4:7], s62 offen lds
	s_waitcnt vmcnt(8)
	s_waitcnt lgkmcnt(0)
	s_barrier
	s_waitcnt lgkmcnt(7)
	v_mfma_f32_16x16x32_bf16 v[66:69], v[140:143], v[172:175], v[66:69]
	v_mfma_f32_16x16x32_bf16 v[62:65], v[148:151], v[172:175], v[62:65]
	s_waitcnt lgkmcnt(5)
	v_mfma_f32_16x16x32_bf16 v[58:61], v[140:143], v[180:183], v[58:61]
	v_mfma_f32_16x16x32_bf16 v[54:57], v[148:151], v[180:183], v[54:57]
	s_waitcnt lgkmcnt(3)
	v_mfma_f32_16x16x32_bf16 v[50:53], v[140:143], v[188:191], v[50:53]
	v_mfma_f32_16x16x32_bf16 v[46:49], v[148:151], v[188:191], v[46:49]
	s_waitcnt lgkmcnt(1)
	v_mfma_f32_16x16x32_bf16 v[42:45], v[140:143], v[196:199], v[42:45]
	v_mfma_f32_16x16x32_bf16 v[38:41], v[148:151], v[196:199], v[38:41]
	v_mfma_f32_16x16x32_bf16 v[66:69], v[144:147], v[176:179], v[66:69]
	v_mfma_f32_16x16x32_bf16 v[62:65], v[152:155], v[176:179], v[62:65]
	v_mfma_f32_16x16x32_bf16 v[58:61], v[144:147], v[184:187], v[58:61]
	v_mfma_f32_16x16x32_bf16 v[54:57], v[152:155], v[184:187], v[54:57]
	v_mfma_f32_16x16x32_bf16 v[50:53], v[144:147], v[192:195], v[50:53]
	v_mfma_f32_16x16x32_bf16 v[46:49], v[152:155], v[192:195], v[46:49]
	s_waitcnt lgkmcnt(0)
	v_mfma_f32_16x16x32_bf16 v[42:45], v[144:147], v[200:203], v[42:45]
	v_mfma_f32_16x16x32_bf16 v[38:41], v[152:155], v[200:203], v[38:41]
	v_mfma_f32_16x16x32_bf16 v[34:37], v[156:159], v[172:175], v[34:37]
	v_mfma_f32_16x16x32_bf16 v[30:33], v[164:167], v[172:175], v[30:33]
	v_mfma_f32_16x16x32_bf16 v[26:29], v[156:159], v[180:183], v[26:29]
	v_mfma_f32_16x16x32_bf16 v[22:25], v[164:167], v[180:183], v[22:25]
	v_mfma_f32_16x16x32_bf16 v[18:21], v[156:159], v[188:191], v[18:21]
	v_mfma_f32_16x16x32_bf16 v[14:17], v[164:167], v[188:191], v[14:17]
	v_mfma_f32_16x16x32_bf16 v[10:13], v[156:159], v[196:199], v[10:13]
	v_mfma_f32_16x16x32_bf16 v[4:7], v[164:167], v[196:199], v[6:9]
	v_mfma_f32_16x16x32_bf16 v[34:37], v[160:163], v[176:179], v[34:37]
	v_mfma_f32_16x16x32_bf16 v[30:33], v[168:171], v[176:179], v[30:33]
	v_mfma_f32_16x16x32_bf16 v[26:29], v[160:163], v[184:187], v[26:29]
	v_mfma_f32_16x16x32_bf16 v[22:25], v[168:171], v[184:187], v[22:25]
	v_mfma_f32_16x16x32_bf16 v[18:21], v[160:163], v[192:195], v[18:21]
	v_mfma_f32_16x16x32_bf16 v[14:17], v[168:171], v[192:195], v[14:17]
	v_mfma_f32_16x16x32_bf16 v[10:13], v[160:163], v[200:203], v[10:13]
	v_mfma_f32_16x16x32_bf16 v[4:7], v[168:171], v[200:203], v[4:7]
	s_barrier
	v_add_u32_e32 v3, 0x18000, v209
	ds_read_b128 v[140:143], v3
	ds_read_b128 v[144:147], v3 offset:1024
	ds_read_b128 v[148:151], v3 offset:2048
	ds_read_b128 v[152:155], v3 offset:3072
	v_add_u32_e32 v3, 0x1c000, v209
	ds_read_b128 v[156:159], v3
	ds_read_b128 v[160:163], v3 offset:1024
	ds_read_b128 v[164:167], v3 offset:2048
	ds_read_b128 v[168:171], v3 offset:3072
	s_add_i32 s62, s62, 0x80000
	s_mov_b32 m0, s34
	ds_read_b128 v[172:175], v210 offset:32768
	ds_read_b128 v[176:179], v210 offset:33792
	ds_read_b128 v[180:183], v210 offset:34816
	ds_read_b128 v[184:187], v210 offset:35840
	ds_read_b128 v[188:191], v210 offset:36864
	ds_read_b128 v[192:195], v210 offset:37888
	ds_read_b128 v[196:199], v210 offset:38912
	ds_read_b128 v[200:203], v210 offset:39936
	buffer_load_dwordx4 v1, s[4:7], s62 offen lds
	s_mov_b32 m0, s35
	s_nop 0
	buffer_load_dwordx4 v206, s[4:7], s62 offen lds
	s_waitcnt vmcnt(8)
	s_waitcnt lgkmcnt(0)
	s_barrier
	s_waitcnt lgkmcnt(7)
	v_mfma_f32_16x16x32_bf16 v[130:133], v[140:143], v[172:175], v[130:133]
	v_mfma_f32_16x16x32_bf16 v[126:129], v[148:151], v[172:175], v[126:129]
	s_waitcnt lgkmcnt(5)
	v_mfma_f32_16x16x32_bf16 v[122:125], v[140:143], v[180:183], v[122:125]
	v_mfma_f32_16x16x32_bf16 v[118:121], v[148:151], v[180:183], v[118:121]
	s_waitcnt lgkmcnt(3)
	v_mfma_f32_16x16x32_bf16 v[114:117], v[140:143], v[188:191], v[114:117]
	v_mfma_f32_16x16x32_bf16 v[110:113], v[148:151], v[188:191], v[110:113]
	s_waitcnt lgkmcnt(1)
	v_mfma_f32_16x16x32_bf16 v[106:109], v[140:143], v[196:199], v[106:109]
	v_mfma_f32_16x16x32_bf16 v[102:105], v[148:151], v[196:199], v[102:105]
	v_mfma_f32_16x16x32_bf16 v[130:133], v[144:147], v[176:179], v[130:133]
	v_mfma_f32_16x16x32_bf16 v[126:129], v[152:155], v[176:179], v[126:129]
	v_mfma_f32_16x16x32_bf16 v[122:125], v[144:147], v[184:187], v[122:125]
	v_mfma_f32_16x16x32_bf16 v[118:121], v[152:155], v[184:187], v[118:121]
	v_mfma_f32_16x16x32_bf16 v[114:117], v[144:147], v[192:195], v[114:117]
	v_mfma_f32_16x16x32_bf16 v[110:113], v[152:155], v[192:195], v[110:113]
	s_waitcnt lgkmcnt(0)
	v_mfma_f32_16x16x32_bf16 v[106:109], v[144:147], v[200:203], v[106:109]
	v_mfma_f32_16x16x32_bf16 v[102:105], v[152:155], v[200:203], v[102:105]
	v_mfma_f32_16x16x32_bf16 v[98:101], v[156:159], v[172:175], v[98:101]
	v_mfma_f32_16x16x32_bf16 v[94:97], v[164:167], v[172:175], v[94:97]
	v_mfma_f32_16x16x32_bf16 v[90:93], v[156:159], v[180:183], v[90:93]
	v_mfma_f32_16x16x32_bf16 v[86:89], v[164:167], v[180:183], v[86:89]
	v_mfma_f32_16x16x32_bf16 v[82:85], v[156:159], v[188:191], v[82:85]
	v_mfma_f32_16x16x32_bf16 v[78:81], v[164:167], v[188:191], v[78:81]
	v_mfma_f32_16x16x32_bf16 v[74:77], v[156:159], v[196:199], v[74:77]
	v_mfma_f32_16x16x32_bf16 v[70:73], v[164:167], v[196:199], v[70:73]
	v_mfma_f32_16x16x32_bf16 v[98:101], v[160:163], v[176:179], v[98:101]
	v_mfma_f32_16x16x32_bf16 v[94:97], v[168:171], v[176:179], v[94:97]
	v_mfma_f32_16x16x32_bf16 v[90:93], v[160:163], v[184:187], v[90:93]
	v_mfma_f32_16x16x32_bf16 v[86:89], v[168:171], v[184:187], v[86:89]
	v_mfma_f32_16x16x32_bf16 v[82:85], v[160:163], v[192:195], v[82:85]
	v_mfma_f32_16x16x32_bf16 v[78:81], v[168:171], v[192:195], v[78:81]
	v_mfma_f32_16x16x32_bf16 v[74:77], v[160:163], v[200:203], v[74:77]
	v_mfma_f32_16x16x32_bf16 v[70:73], v[168:171], v[200:203], v[70:73]
	s_barrier
	s_mov_b32 m0, s38
	s_add_i32 s62, s61, 0x80
	ds_read_b128 v[172:175], v210 offset:49152
	ds_read_b128 v[176:179], v210 offset:50176
	ds_read_b128 v[180:183], v210 offset:51200
	ds_read_b128 v[184:187], v210 offset:52224
	ds_read_b128 v[188:191], v210 offset:53248
	ds_read_b128 v[192:195], v210 offset:54272
	ds_read_b128 v[196:199], v210 offset:55296
	ds_read_b128 v[200:203], v210 offset:56320
	buffer_load_dwordx4 v135, s[8:11], s62 offen lds
	s_mov_b32 m0, s39
	s_add_i32 s61, s61, 0x80080
	buffer_load_dwordx4 v207, s[8:11], s62 offen lds
	s_mov_b32 m0, s42
	s_nop 0
	buffer_load_dwordx4 v135, s[8:11], s61 offen lds
	s_mov_b32 m0, s43
	s_nop 0
	buffer_load_dwordx4 v207, s[8:11], s61 offen lds
	s_mov_b32 m0, s40
	s_nop 0
	buffer_load_dwordx4 v1, s[4:7], s60 offen lds
	s_mov_b32 m0, s41
	s_nop 0
	buffer_load_dwordx4 v206, s[4:7], s60 offen lds
	s_waitcnt vmcnt(8)
	s_waitcnt lgkmcnt(0)
	s_barrier
	s_waitcnt lgkmcnt(7)
	v_mfma_f32_16x16x32_bf16 v[66:69], v[140:143], v[172:175], v[66:69]
	v_mfma_f32_16x16x32_bf16 v[62:65], v[148:151], v[172:175], v[62:65]
	s_waitcnt lgkmcnt(5)
	v_mfma_f32_16x16x32_bf16 v[58:61], v[140:143], v[180:183], v[58:61]
	v_mfma_f32_16x16x32_bf16 v[54:57], v[148:151], v[180:183], v[54:57]
	s_waitcnt lgkmcnt(3)
	v_mfma_f32_16x16x32_bf16 v[50:53], v[140:143], v[188:191], v[50:53]
	v_mfma_f32_16x16x32_bf16 v[46:49], v[148:151], v[188:191], v[46:49]
	s_waitcnt lgkmcnt(1)
	v_mfma_f32_16x16x32_bf16 v[42:45], v[140:143], v[196:199], v[42:45]
	v_mfma_f32_16x16x32_bf16 v[38:41], v[148:151], v[196:199], v[38:41]
	v_mfma_f32_16x16x32_bf16 v[66:69], v[144:147], v[176:179], v[66:69]
	v_mfma_f32_16x16x32_bf16 v[62:65], v[152:155], v[176:179], v[62:65]
	v_mfma_f32_16x16x32_bf16 v[58:61], v[144:147], v[184:187], v[58:61]
	v_mfma_f32_16x16x32_bf16 v[54:57], v[152:155], v[184:187], v[54:57]
	v_mfma_f32_16x16x32_bf16 v[50:53], v[144:147], v[192:195], v[50:53]
	v_mfma_f32_16x16x32_bf16 v[46:49], v[152:155], v[192:195], v[46:49]
	s_waitcnt lgkmcnt(0)
	v_mfma_f32_16x16x32_bf16 v[42:45], v[144:147], v[200:203], v[42:45]
	v_mfma_f32_16x16x32_bf16 v[38:41], v[152:155], v[200:203], v[38:41]
	v_mfma_f32_16x16x32_bf16 v[34:37], v[156:159], v[172:175], v[34:37]
	v_mfma_f32_16x16x32_bf16 v[30:33], v[164:167], v[172:175], v[30:33]
	v_mfma_f32_16x16x32_bf16 v[26:29], v[156:159], v[180:183], v[26:29]
	v_mfma_f32_16x16x32_bf16 v[22:25], v[164:167], v[180:183], v[22:25]
	v_mfma_f32_16x16x32_bf16 v[18:21], v[156:159], v[188:191], v[18:21]
	v_mfma_f32_16x16x32_bf16 v[14:17], v[164:167], v[188:191], v[14:17]
	v_mfma_f32_16x16x32_bf16 v[8:11], v[156:159], v[196:199], v[10:13]
	v_mfma_f32_16x16x32_bf16 v[4:7], v[164:167], v[196:199], v[4:7]
	v_mfma_f32_16x16x32_bf16 v[34:37], v[160:163], v[176:179], v[34:37]
	v_mfma_f32_16x16x32_bf16 v[30:33], v[168:171], v[176:179], v[30:33]
	v_mfma_f32_16x16x32_bf16 v[26:29], v[160:163], v[184:187], v[26:29]
	v_mfma_f32_16x16x32_bf16 v[22:25], v[168:171], v[184:187], v[22:25]
	v_mfma_f32_16x16x32_bf16 v[18:21], v[160:163], v[192:195], v[18:21]
	v_mfma_f32_16x16x32_bf16 v[14:17], v[168:171], v[192:195], v[14:17]
	v_mfma_f32_16x16x32_bf16 v[10:13], v[160:163], v[200:203], v[8:11]
	v_mfma_f32_16x16x32_bf16 v[6:9], v[168:171], v[200:203], v[4:7]
	s_barrier
	s_add_i32 s59, s59, 2
	s_addk_i32 s57, 0x100
	s_addk_i32 s58, 0x100
	s_cmp_gt_u32 s59, 13
	s_cbranch_scc0 .LBB0_563
	s_and_b64 vcc, exec, s[20:21]
	s_cbranch_vccz .LBB0_566
	s_barrier
